# stack10: stack9 + GLA-finish loop touches the next item's rows (L2 prefetch loads into a dead register quad)
# baseline (speedup 1.0000x reference)
.LBB0_817:
	v_mov_b32_e32 v2, v48
	s_nop 0
	v_ashrrev_i32_e32 v3, 31, v2
	v_lshl_add_u64 v[4:5], s[16:17], 0, v[2:3]
	v_lshlrev_b64 v[46:47], 1, v[4:5]
	v_lshl_add_u64 v[4:5], s[6:7], 0, v[46:47]
	v_lshl_add_u64 v[6:7], s[8:9], 0, v[46:47]
	v_lshl_add_u64 v[8:9], v[2:3], 1, s[12:13]
	global_load_dwordx4 v[60:63], v[4:5], off nt
	global_load_dwordx4 v[38:41], v[4:5], off offset:1024 nt
	global_load_dwordx4 v[64:67], v[6:7], off nt
	global_load_dwordx4 v[42:45], v[6:7], off offset:1024 nt
	global_load_dwordx4 v[68:71], v[8:9], off nt
	global_load_dwordx4 v[34:37], v[8:9], off offset:1024 nt
	global_load_dwordx4 v[26:29], v[4:5], off offset:2048 nt
	global_load_dwordx4 v[14:17], v[4:5], off offset:3072 nt
	global_load_dwordx4 v[30:33], v[6:7], off offset:2048 nt
	global_load_dwordx4 v[18:21], v[6:7], off offset:3072 nt
	global_load_dwordx4 v[22:25], v[8:9], off offset:2048 nt
	global_load_dwordx4 v[10:13], v[8:9], off offset:3072 nt
	v_lshl_add_u64 v[6:7], v[2:3], 2, s[22:23]
	global_load_dwordx4 v[2:5], v[6:7], off offset:16
	s_nop 0
	global_load_dwordx4 v[6:9], v[6:7], off
	s_waitcnt vmcnt(13)
	v_lshlrev_b32_e32 v72, 16, v60
	s_waitcnt vmcnt(11)
	v_lshlrev_b32_e32 v73, 16, v64
	v_and_b32_e32 v64, 0xffff0000, v64
	v_and_b32_e32 v60, 0xffff0000, v60
	v_add_f32_e32 v72, v73, v72
	v_add_f32_e32 v73, v64, v60
	v_lshlrev_b32_e32 v60, 16, v61
	v_lshlrev_b32_e32 v64, 16, v65
	v_add_f32_e32 v74, v64, v60
	v_and_b32_e32 v60, 0xffff0000, v65
	v_and_b32_e32 v61, 0xffff0000, v61
	v_add_f32_e32 v65, v60, v61
	v_lshlrev_b32_e32 v60, 16, v62
	v_lshlrev_b32_e32 v61, 16, v66
	v_add_f32_e32 v75, v61, v60
	v_and_b32_e32 v60, 0xffff0000, v66
	v_and_b32_e32 v61, 0xffff0000, v62
	v_add_f32_e32 v76, v60, v61
	v_lshlrev_b32_e32 v60, 16, v63
	v_lshlrev_b32_e32 v61, 16, v67
	v_add_f32_e32 v77, v61, v60
	v_and_b32_e32 v60, 0xffff0000, v67
	v_and_b32_e32 v61, 0xffff0000, v63
	v_add_f32_e32 v78, v60, v61
	v_mul_f32_e32 v60, v72, v72
	v_fmac_f32_e32 v60, v73, v73
	v_fmac_f32_e32 v60, v74, v74
	v_fmac_f32_e32 v60, v65, v65
	v_fmac_f32_e32 v60, v75, v75
	v_cmp_lt_i32_e32 vcc, v51, v50
	v_fmac_f32_e32 v60, v76, v76
	v_fmac_f32_e32 v60, v77, v77
	v_cndmask_b32_e32 v59, v49, v51, vcc
	v_lshlrev_b32_e32 v59, 2, v59
	v_fmac_f32_e32 v60, v78, v78
	s_nop 1
	v_mov_b32_dpp v61, v60 quad_perm:[1,0,3,2] row_mask:0xf bank_mask:0xf
	v_cmp_lt_i32_e32 vcc, v52, v50
	v_lshl_add_u64 v[46:47], s[10:11], 0, v[46:47]
	s_add_i32 s20, s20, s92
	v_cndmask_b32_e32 v62, v49, v52, vcc
	v_lshlrev_b32_e32 v64, 2, v62
	s_waitcnt lgkmcnt(0)
	v_add_f32_e32 v60, v60, v61
	s_nop 1
	v_mov_b32_dpp v61, v60 quad_perm:[2,3,0,1] row_mask:0xf bank_mask:0xf
	v_cmp_lt_i32_e32 vcc, v53, v50
	s_add_u32 s12, s12, s14
	s_addc_u32 s13, s13, s15
	v_cndmask_b32_e32 v62, v49, v53, vcc
	v_lshlrev_b32_e32 v63, 2, v62
	s_waitcnt lgkmcnt(0)
	v_add_f32_e32 v61, v60, v61
	s_nop 1
	v_mov_b32_dpp v62, v61 row_half_mirror row_mask:0xf bank_mask:0xf
	v_cmp_lt_i32_e32 vcc, v54, v50
	s_add_u32 s16, s16, s18
	s_addc_u32 s17, s17, s19
	v_cndmask_b32_e32 v60, v49, v54, vcc
	v_lshlrev_b32_e32 v60, 2, v60
	s_waitcnt lgkmcnt(0)
	v_add_f32_e32 v62, v61, v62
	s_nop 1
	v_mov_b32_dpp v66, v62 row_mirror row_mask:0xf bank_mask:0xf
	v_cmp_lt_i32_e32 vcc, v55, v50
	s_cmpk_lt_i32 s20, 0x4400
	s_waitcnt lgkmcnt(0)
	v_add_f32_e32 v66, v62, v66
	v_cndmask_b32_e32 v61, v49, v55, vcc
	v_lshlrev_b32_e32 v61, 2, v61
	v_mov_b32_e32 v67, v66
	v_mov_b32_e32 v61, v66
	s_nop 1
	v_permlane16_swap_b32_e32 v67, v61
	s_nop 1
	v_mov_b32_dpp v67, v61 quad_perm:[0,1,2,3] row_mask:0x5 bank_mask:0xf
	v_cmp_lt_i32_e32 vcc, v56, v50
	s_waitcnt lgkmcnt(0)
	v_add_f32_e32 v66, v66, v67
	v_cndmask_b32_e32 v62, v49, v56, vcc
	v_lshlrev_b32_e32 v62, 2, v62
	v_mov_b32_e32 v67, v66
	v_mov_b32_e32 v62, v66
	s_nop 1
	v_permlane32_swap_b32_e32 v67, v62
	s_nop 1
	v_mov_b32_dpp v67, v62 quad_perm:[0,1,2,3] row_mask:0x3 bank_mask:0xf
	s_waitcnt lgkmcnt(0)
	v_add_f32_e32 v66, v66, v67
	v_fmamk_f32 v66, v66, 0x3b000000, v57
	v_mul_f32_e32 v67, 0x4f800000, v66
	v_cmp_gt_f32_e32 vcc, s2, v66
	s_nop 1
	v_cndmask_b32_e32 v66, v66, v67, vcc
	v_sqrt_f32_e32 v67, v66
	s_nop 0
	v_add_u32_e32 v79, -1, v67
	v_fma_f32 v80, -v79, v67, v66
	v_cmp_ge_f32_e64 s[0:1], 0, v80
	v_add_u32_e32 v80, 1, v67
	s_nop 0
	v_cndmask_b32_e64 v79, v67, v79, s[0:1]
	v_fma_f32 v67, -v80, v67, v66
	v_cmp_lt_f32_e64 s[0:1], 0, v67
	s_nop 1
	v_cndmask_b32_e64 v67, v79, v80, s[0:1]
	v_mul_f32_e32 v79, 0x37800000, v67
	v_cndmask_b32_e32 v67, v67, v79, vcc
	v_cmp_class_f32_e32 vcc, v66, v58
	s_nop 1
	v_cndmask_b32_e32 v66, v67, v66, vcc
	v_div_scale_f32 v67, s[0:1], v66, v66, 1.0
	v_rcp_f32_e32 v79, v67
	s_nop 0
	v_fma_f32 v80, -v67, v79, 1.0
	v_fmac_f32_e32 v79, v80, v79
	v_div_scale_f32 v80, vcc, 1.0, v66, 1.0
	v_mul_f32_e32 v81, v80, v79
	v_fma_f32 v82, -v67, v81, v80
	v_fmac_f32_e32 v81, v82, v79
	v_fma_f32 v67, -v67, v81, v80
	v_div_fmas_f32 v67, v67, v79, v81
	v_div_fixup_f32 v79, v67, v66, 1.0
	s_waitcnt vmcnt(9)
	v_lshlrev_b32_e32 v66, 16, v68
	v_mul_f32_e32 v80, 0xbfb8aa3b, v66
	v_exp_f32_e32 v80, v80
	v_and_b32_e32 v67, 0xffff0000, v68
	v_mul_f32_e32 v72, v72, v79
	s_waitcnt vmcnt(0)
	s_cbranch_scc0 .Lpf5_skip
	v_mov_b32_e32 v100, v48
	v_ashrrev_i32_e32 v101, 31, v48
	v_lshl_add_u64 v[102:103], s[16:17], 0, v[100:101]
	v_lshlrev_b64 v[102:103], 1, v[102:103]
	v_lshl_add_u64 v[104:105], s[6:7], 0, v[102:103]
	v_lshl_add_u64 v[106:107], s[8:9], 0, v[102:103]
	v_lshl_add_u64 v[108:109], v[100:101], 1, s[12:13]
	global_load_dwordx4 v[110:113], v[104:105], off
	global_load_dwordx4 v[110:113], v[104:105], off offset:1024
	global_load_dwordx4 v[110:113], v[104:105], off offset:2048
	global_load_dwordx4 v[110:113], v[104:105], off offset:3072
	global_load_dwordx4 v[110:113], v[106:107], off
	global_load_dwordx4 v[110:113], v[106:107], off offset:1024
	global_load_dwordx4 v[110:113], v[106:107], off offset:2048
	global_load_dwordx4 v[110:113], v[106:107], off offset:3072
	global_load_dwordx4 v[110:113], v[108:109], off
	global_load_dwordx4 v[110:113], v[108:109], off offset:1024
	global_load_dwordx4 v[110:113], v[108:109], off offset:2048
	global_load_dwordx4 v[110:113], v[108:109], off offset:3072
.Lpf5_skip:
	v_mul_f32_e32 v72, v6, v72
	v_add_f32_e32 v80, 1.0, v80
	v_div_scale_f32 v83, s[0:1], v80, v80, v66
	v_rcp_f32_e32 v84, v83
	v_lshlrev_b32_e32 v68, 16, v69
	v_and_b32_e32 v69, 0xffff0000, v69
	v_lshlrev_b32_e32 v81, 16, v70
	v_fma_f32 v85, -v83, v84, 1.0
	v_fmac_f32_e32 v84, v85, v84
	v_div_scale_f32 v85, vcc, v66, v80, v66
	v_mul_f32_e32 v86, v85, v84
	v_fma_f32 v87, -v83, v86, v85
	v_fmac_f32_e32 v86, v87, v84
	v_fma_f32 v83, -v83, v86, v85
	v_mul_f32_e32 v85, 0xbfb8aa3b, v67
	v_exp_f32_e32 v85, v85
	v_div_fmas_f32 v83, v83, v84, v86
	v_div_fixup_f32 v66, v83, v80, v66
	v_mul_f32_e32 v66, v66, v72
	v_add_f32_e32 v80, 1.0, v85
	v_div_scale_f32 v83, s[0:1], v80, v80, v67
	v_rcp_f32_e32 v84, v83
	v_mul_f32_e32 v72, v73, v79
	v_mul_f32_e32 v72, v7, v72
	v_mul_f32_e32 v65, v65, v79
	v_fma_f32 v73, -v83, v84, 1.0
	v_fmac_f32_e32 v84, v73, v84
	v_div_scale_f32 v73, vcc, v67, v80, v67
	v_mul_f32_e32 v85, v73, v84
	v_fma_f32 v86, -v83, v85, v73
	v_fmac_f32_e32 v85, v86, v84
	v_fma_f32 v73, -v83, v85, v73
	v_mul_f32_e32 v83, 0xbfb8aa3b, v68
	v_exp_f32_e32 v83, v83
	v_div_fmas_f32 v73, v73, v84, v85
	v_div_fixup_f32 v67, v73, v80, v67
	v_mul_f32_e32 v67, v67, v72
	v_add_f32_e32 v72, 1.0, v83
	v_div_scale_f32 v73, s[0:1], v72, v72, v68
	v_rcp_f32_e32 v80, v73
	v_cvt_pk_bf16_f32 v66, v66, v67
	v_mul_f32_e32 v67, v74, v79
	v_mul_f32_e32 v67, v8, v67
	v_fma_f32 v74, -v73, v80, 1.0
	v_fmac_f32_e32 v80, v74, v80
	v_div_scale_f32 v74, vcc, v68, v72, v68
	v_mul_f32_e32 v83, v74, v80
	v_fma_f32 v84, -v73, v83, v74
	v_fmac_f32_e32 v83, v84, v80
	v_fma_f32 v73, -v73, v83, v74
	v_mul_f32_e32 v74, 0xbfb8aa3b, v69
	v_exp_f32_e32 v74, v74
	v_div_fmas_f32 v73, v73, v80, v83
	v_div_fixup_f32 v68, v73, v72, v68
	v_mul_f32_e32 v67, v68, v67
	v_add_f32_e32 v72, 1.0, v74
	v_div_scale_f32 v73, s[0:1], v72, v72, v69
	v_rcp_f32_e32 v74, v73
	v_mul_f32_e32 v65, v9, v65
	v_and_b32_e32 v70, 0xffff0000, v70
	v_lshlrev_b32_e32 v82, 16, v71
	v_fma_f32 v68, -v73, v74, 1.0
	v_fmac_f32_e32 v74, v68, v74
	v_div_scale_f32 v68, vcc, v69, v72, v69
	v_mul_f32_e32 v80, v68, v74
	v_fma_f32 v83, -v73, v80, v68
	v_fmac_f32_e32 v80, v83, v74
	v_fma_f32 v68, -v73, v80, v68
	v_mul_f32_e32 v73, 0xbfb8aa3b, v81
	v_exp_f32_e32 v73, v73
	v_div_fmas_f32 v68, v68, v74, v80
	v_div_fixup_f32 v68, v68, v72, v69
	v_mul_f32_e32 v65, v68, v65
	v_add_f32_e32 v68, 1.0, v73
	v_div_scale_f32 v69, s[0:1], v68, v68, v81
	v_rcp_f32_e32 v72, v69
	v_cvt_pk_bf16_f32 v67, v67, v65
	v_mul_f32_e32 v65, v75, v79
	v_mul_f32_e32 v65, v2, v65
	v_fma_f32 v73, -v69, v72, 1.0
	v_fmac_f32_e32 v72, v73, v72
	v_div_scale_f32 v73, vcc, v81, v68, v81
	v_mul_f32_e32 v74, v73, v72
	v_fma_f32 v75, -v69, v74, v73
	v_fmac_f32_e32 v74, v75, v72
	v_fma_f32 v69, -v69, v74, v73
	v_mul_f32_e32 v73, 0xbfb8aa3b, v70
	v_exp_f32_e32 v73, v73
	v_div_fmas_f32 v69, v69, v72, v74
	v_div_fixup_f32 v68, v69, v68, v81
	v_mul_f32_e32 v65, v68, v65
	v_add_f32_e32 v69, 1.0, v73
	v_div_scale_f32 v72, s[0:1], v69, v69, v70
	v_rcp_f32_e32 v73, v72
	v_mul_f32_e32 v68, v76, v79
	v_mul_f32_e32 v68, v3, v68
	v_and_b32_e32 v71, 0xffff0000, v71
	v_fma_f32 v74, -v72, v73, 1.0
	v_fmac_f32_e32 v73, v74, v73
	v_div_scale_f32 v74, vcc, v70, v69, v70
	v_mul_f32_e32 v75, v74, v73
	v_fma_f32 v76, -v72, v75, v74
	v_fmac_f32_e32 v75, v76, v73
	v_fma_f32 v72, -v72, v75, v74
	v_mul_f32_e32 v74, 0xbfb8aa3b, v82
	v_exp_f32_e32 v74, v74
	v_div_fmas_f32 v72, v72, v73, v75
	v_div_fixup_f32 v69, v72, v69, v70
	v_mul_f32_e32 v68, v69, v68
	v_add_f32_e32 v69, 1.0, v74
	v_lshlrev_b32_e32 v74, 16, v38
	v_lshlrev_b32_e32 v75, 16, v42
	v_and_b32_e32 v42, 0xffff0000, v42
	v_and_b32_e32 v38, 0xffff0000, v38
	v_add_f32_e32 v74, v75, v74
	v_add_f32_e32 v38, v42, v38
	v_lshlrev_b32_e32 v42, 16, v39
	v_lshlrev_b32_e32 v75, 16, v43
	v_and_b32_e32 v43, 0xffff0000, v43
	v_and_b32_e32 v39, 0xffff0000, v39
	v_add_f32_e32 v42, v75, v42
	v_add_f32_e32 v39, v43, v39
	v_lshlrev_b32_e32 v43, 16, v40
	v_lshlrev_b32_e32 v75, 16, v44
	v_and_b32_e32 v44, 0xffff0000, v44
	v_and_b32_e32 v40, 0xffff0000, v40
	v_add_f32_e32 v43, v75, v43
	v_add_f32_e32 v40, v44, v40
	v_lshlrev_b32_e32 v44, 16, v41
	v_lshlrev_b32_e32 v75, 16, v45
	v_and_b32_e32 v45, 0xffff0000, v45
	v_and_b32_e32 v41, 0xffff0000, v41
	v_add_f32_e32 v41, v45, v41
	v_mul_f32_e32 v45, v74, v74
	v_fmac_f32_e32 v45, v38, v38
	v_fmac_f32_e32 v45, v42, v42
	v_fmac_f32_e32 v45, v39, v39
	v_div_scale_f32 v70, s[0:1], v69, v69, v82
	v_fmac_f32_e32 v45, v43, v43
	v_rcp_f32_e32 v72, v70
	v_add_f32_e32 v44, v75, v44
	v_fmac_f32_e32 v45, v40, v40
	v_fmac_f32_e32 v45, v44, v44
	v_fmac_f32_e32 v45, v41, v41
	s_nop 1
	v_mov_b32_dpp v75, v45 quad_perm:[1,0,3,2] row_mask:0xf bank_mask:0xf
	v_fma_f32 v73, -v70, v72, 1.0
	v_fmac_f32_e32 v72, v73, v72
	v_div_scale_f32 v73, vcc, v82, v69, v82
	v_mul_f32_e32 v76, v73, v72
	v_cvt_pk_bf16_f32 v68, v65, v68
	v_mul_f32_e32 v65, v77, v79
	v_fma_f32 v77, -v70, v76, v73
	v_fmac_f32_e32 v76, v77, v72
	s_waitcnt lgkmcnt(0)
	v_add_f32_e32 v45, v45, v75
	v_fma_f32 v70, -v70, v76, v73
	s_nop 1
	v_mov_b32_dpp v73, v45 quad_perm:[2,3,0,1] row_mask:0xf bank_mask:0xf
	v_div_fmas_f32 v70, v70, v72, v76
	v_mul_f32_e32 v72, 0xbfb8aa3b, v71
	v_exp_f32_e32 v72, v72
	v_div_fixup_f32 v69, v70, v69, v82
	s_waitcnt lgkmcnt(0)
	v_add_f32_e32 v45, v45, v73
	s_nop 1
	v_mov_b32_dpp v73, v45 row_half_mirror row_mask:0xf bank_mask:0xf
	v_add_f32_e32 v70, 1.0, v72
	v_mul_f32_e32 v65, v4, v65
	v_mul_f32_e32 v65, v69, v65
	v_mul_f32_e32 v69, v78, v79
	s_waitcnt lgkmcnt(0)
	v_add_f32_e32 v45, v45, v73
	s_nop 1
	v_mov_b32_dpp v72, v45 row_mirror row_mask:0xf bank_mask:0xf
	v_div_scale_f32 v73, s[0:1], v70, v70, v71
	v_rcp_f32_e32 v75, v73
	v_mul_f32_e32 v69, v5, v69
	s_waitcnt lgkmcnt(0)
	v_add_f32_e32 v45, v45, v72
	v_mov_b32_e32 v72, v45
	v_mov_b32_e32 v61, v45
	s_nop 1
	v_permlane16_swap_b32_e32 v72, v61
	s_nop 1
	v_mov_b32_dpp v72, v61 quad_perm:[0,1,2,3] row_mask:0x5 bank_mask:0xf
	v_fma_f32 v76, -v73, v75, 1.0
	v_fmac_f32_e32 v75, v76, v75
	v_div_scale_f32 v76, vcc, v71, v70, v71
	s_waitcnt lgkmcnt(0)
	v_add_f32_e32 v45, v45, v72
	v_mov_b32_e32 v72, v45
	v_mov_b32_e32 v62, v45
	s_nop 1
	v_permlane32_swap_b32_e32 v72, v62
	s_nop 1
	v_mov_b32_dpp v72, v62 quad_perm:[0,1,2,3] row_mask:0x3 bank_mask:0xf
	v_mul_f32_e32 v77, v76, v75
	v_fma_f32 v78, -v73, v77, v76
	v_fmac_f32_e32 v77, v78, v75
	v_fma_f32 v73, -v73, v77, v76
	s_waitcnt lgkmcnt(0)
	v_add_f32_e32 v45, v45, v72
	v_fmamk_f32 v45, v45, 0x3b000000, v57
	v_mul_f32_e32 v72, 0x4f800000, v45
	v_cmp_gt_f32_e64 s[0:1], s2, v45
	v_div_fmas_f32 v73, v73, v75, v77
	v_div_fixup_f32 v70, v73, v70, v71
	v_cndmask_b32_e64 v45, v45, v72, s[0:1]
	v_sqrt_f32_e32 v72, v45
	v_mul_f32_e32 v69, v70, v69
	v_cvt_pk_bf16_f32 v69, v65, v69
	global_store_dwordx4 v[46:47], v[66:69], off
	v_add_u32_e32 v71, -1, v72
	v_fma_f32 v73, -v71, v72, v45
	v_cmp_ge_f32_e32 vcc, 0, v73
	v_add_u32_e32 v73, 1, v72
	v_lshlrev_b32_e32 v68, 16, v36
	v_cndmask_b32_e32 v71, v72, v71, vcc
	v_fma_f32 v72, -v73, v72, v45
	v_cmp_lt_f32_e32 vcc, 0, v72
	v_and_b32_e32 v36, 0xffff0000, v36
	v_lshlrev_b32_e32 v69, 16, v37
	v_cndmask_b32_e32 v71, v71, v73, vcc
	v_mul_f32_e32 v72, 0x37800000, v71
	v_cndmask_b32_e64 v71, v71, v72, s[0:1]
	v_cmp_class_f32_e32 vcc, v45, v58
	v_and_b32_e32 v37, 0xffff0000, v37
	s_nop 0
	v_cndmask_b32_e32 v45, v71, v45, vcc
	v_div_scale_f32 v71, s[0:1], v45, v45, 1.0
	v_rcp_f32_e32 v72, v71
	s_nop 0
	v_fma_f32 v65, -v71, v72, 1.0
	v_fmac_f32_e32 v72, v65, v72
	v_div_scale_f32 v65, vcc, 1.0, v45, 1.0
	v_mul_f32_e32 v66, v65, v72
	v_fma_f32 v67, -v71, v66, v65
	v_fmac_f32_e32 v66, v67, v72
	v_fma_f32 v65, -v71, v66, v65
	v_div_fmas_f32 v65, v65, v72, v66
	v_div_fixup_f32 v45, v65, v45, 1.0
	v_lshlrev_b32_e32 v65, 16, v34
	v_mul_f32_e32 v67, 0xbfb8aa3b, v65
	v_exp_f32_e32 v67, v67
	v_mul_f32_e32 v72, v74, v45
	v_and_b32_e32 v34, 0xffff0000, v34
	v_mul_f32_e32 v72, v6, v72
	v_add_f32_e32 v67, 1.0, v67
	v_div_scale_f32 v70, s[0:1], v67, v67, v65
	v_rcp_f32_e32 v71, v70
	v_lshlrev_b32_e32 v66, 16, v35
	v_mul_f32_e32 v38, v38, v45
	v_mul_f32_e32 v38, v7, v38
	v_fma_f32 v73, -v70, v71, 1.0
	v_fmac_f32_e32 v71, v73, v71
	v_div_scale_f32 v73, vcc, v65, v67, v65
	v_mul_f32_e32 v74, v73, v71
	v_fma_f32 v75, -v70, v74, v73
	v_fmac_f32_e32 v74, v75, v71
	v_fma_f32 v70, -v70, v74, v73
	v_mul_f32_e32 v73, 0xbfb8aa3b, v34
	v_exp_f32_e32 v73, v73
	v_div_fmas_f32 v70, v70, v71, v74
	v_div_fixup_f32 v65, v70, v67, v65
	v_mul_f32_e32 v65, v65, v72
	v_add_f32_e32 v67, 1.0, v73
	v_div_scale_f32 v70, s[0:1], v67, v67, v34
	v_rcp_f32_e32 v71, v70
	v_and_b32_e32 v35, 0xffff0000, v35
	v_mul_f32_e32 v42, v42, v45
	v_mul_f32_e32 v42, v8, v42
	v_fma_f32 v72, -v70, v71, 1.0
	v_fmac_f32_e32 v71, v72, v71
	v_div_scale_f32 v72, vcc, v34, v67, v34
	v_mul_f32_e32 v73, v72, v71
	v_fma_f32 v74, -v70, v73, v72
	v_fmac_f32_e32 v73, v74, v71
	v_fma_f32 v70, -v70, v73, v72
	v_mul_f32_e32 v72, 0xbfb8aa3b, v66
	v_exp_f32_e32 v72, v72
	v_div_fmas_f32 v70, v70, v71, v73
	v_div_fixup_f32 v34, v70, v67, v34
	v_mul_f32_e32 v34, v34, v38
	v_add_f32_e32 v38, 1.0, v72
	v_div_scale_f32 v67, s[0:1], v38, v38, v66
	v_rcp_f32_e32 v70, v67
	v_cvt_pk_bf16_f32 v34, v65, v34
	v_mul_f32_e32 v39, v39, v45
	v_mul_f32_e32 v39, v9, v39
	v_fma_f32 v65, -v67, v70, 1.0
	v_fmac_f32_e32 v70, v65, v70
	v_div_scale_f32 v65, vcc, v66, v38, v66
	v_mul_f32_e32 v71, v65, v70
	v_fma_f32 v72, -v67, v71, v65
	v_fmac_f32_e32 v71, v72, v70
	v_fma_f32 v65, -v67, v71, v65
	v_mul_f32_e32 v67, 0xbfb8aa3b, v35
	v_exp_f32_e32 v67, v67
	v_div_fmas_f32 v65, v65, v70, v71
	v_div_fixup_f32 v38, v65, v38, v66
	v_mul_f32_e32 v38, v38, v42
	v_add_f32_e32 v65, 1.0, v67
	v_div_scale_f32 v66, s[0:1], v65, v65, v35
	v_rcp_f32_e32 v67, v66
	s_nop 0
	v_fma_f32 v42, -v66, v67, 1.0
	v_fmac_f32_e32 v67, v42, v67
	v_div_scale_f32 v42, vcc, v35, v65, v35
	v_mul_f32_e32 v70, v42, v67
	v_fma_f32 v71, -v66, v70, v42
	v_fmac_f32_e32 v70, v71, v67
	v_fma_f32 v42, -v66, v70, v42
	v_mul_f32_e32 v66, 0xbfb8aa3b, v68
	v_exp_f32_e32 v66, v66
	v_div_fmas_f32 v42, v42, v67, v70
	v_div_fixup_f32 v35, v42, v65, v35
	v_mul_f32_e32 v35, v35, v39
	v_add_f32_e32 v39, 1.0, v66
	v_div_scale_f32 v42, s[0:1], v39, v39, v68
	v_rcp_f32_e32 v65, v42
	v_cvt_pk_bf16_f32 v35, v38, v35
	v_mul_f32_e32 v38, v43, v45
	v_mul_f32_e32 v38, v2, v38
	v_fma_f32 v43, -v42, v65, 1.0
	v_fmac_f32_e32 v65, v43, v65
	v_div_scale_f32 v43, vcc, v68, v39, v68
	v_mul_f32_e32 v66, v43, v65
	v_fma_f32 v67, -v42, v66, v43
	v_fmac_f32_e32 v66, v67, v65
	v_fma_f32 v42, -v42, v66, v43
	v_mul_f32_e32 v43, 0xbfb8aa3b, v36
	v_exp_f32_e32 v43, v43
	v_div_fmas_f32 v42, v42, v65, v66
	v_div_fixup_f32 v39, v42, v39, v68
	v_mul_f32_e32 v38, v39, v38
	v_add_f32_e32 v42, 1.0, v43
	v_div_scale_f32 v43, s[0:1], v42, v42, v36
	v_rcp_f32_e32 v65, v43
	v_mul_f32_e32 v39, v40, v45
	v_mul_f32_e32 v39, v3, v39
	v_fma_f32 v40, -v43, v65, 1.0
	v_fmac_f32_e32 v65, v40, v65
	v_div_scale_f32 v40, vcc, v36, v42, v36
	v_mul_f32_e32 v66, v40, v65
	v_fma_f32 v67, -v43, v66, v40
	v_fmac_f32_e32 v66, v67, v65
	v_fma_f32 v40, -v43, v66, v40
	v_div_fmas_f32 v40, v40, v65, v66
	v_div_fixup_f32 v36, v40, v42, v36
	v_mul_f32_e32 v36, v36, v39
	v_cvt_pk_bf16_f32 v36, v38, v36
	v_mul_f32_e32 v38, v44, v45
	v_lshlrev_b32_e32 v44, 16, v26
	v_lshlrev_b32_e32 v65, 16, v30
	v_and_b32_e32 v30, 0xffff0000, v30
	v_and_b32_e32 v26, 0xffff0000, v26
	v_add_f32_e32 v44, v65, v44
	v_add_f32_e32 v26, v30, v26
	v_lshlrev_b32_e32 v30, 16, v27
	v_lshlrev_b32_e32 v65, 16, v31
	v_and_b32_e32 v31, 0xffff0000, v31
	v_and_b32_e32 v27, 0xffff0000, v27
	v_mul_f32_e32 v43, 0xbfb8aa3b, v69
	v_add_f32_e32 v30, v65, v30
	v_add_f32_e32 v27, v31, v27
	v_lshlrev_b32_e32 v31, 16, v28
	v_lshlrev_b32_e32 v65, 16, v32
	v_and_b32_e32 v32, 0xffff0000, v32
	v_and_b32_e32 v28, 0xffff0000, v28
	v_exp_f32_e32 v43, v43
	v_add_f32_e32 v31, v65, v31
	v_add_f32_e32 v28, v32, v28
	v_lshlrev_b32_e32 v32, 16, v29
	v_lshlrev_b32_e32 v65, 16, v33
	v_and_b32_e32 v33, 0xffff0000, v33
	v_and_b32_e32 v29, 0xffff0000, v29
	v_add_f32_e32 v29, v33, v29
	v_mul_f32_e32 v33, v44, v44
	v_fmac_f32_e32 v33, v26, v26
	v_fmac_f32_e32 v33, v30, v30
	v_add_f32_e32 v39, 1.0, v43
	v_fmac_f32_e32 v33, v27, v27
	v_div_scale_f32 v40, s[0:1], v39, v39, v69
	v_fmac_f32_e32 v33, v31, v31
	v_rcp_f32_e32 v42, v40
	v_add_f32_e32 v32, v65, v32
	v_fmac_f32_e32 v33, v28, v28
	v_fmac_f32_e32 v33, v32, v32
	v_fmac_f32_e32 v33, v29, v29
	s_nop 1
	v_mov_b32_dpp v65, v33 quad_perm:[1,0,3,2] row_mask:0xf bank_mask:0xf
	v_fma_f32 v43, -v40, v42, 1.0
	v_fmac_f32_e32 v42, v43, v42
	v_div_scale_f32 v43, vcc, v69, v39, v69
	v_mul_f32_e32 v66, v43, v42
	v_fma_f32 v67, -v40, v66, v43
	v_fmac_f32_e32 v66, v67, v42
	s_waitcnt lgkmcnt(0)
	v_add_f32_e32 v33, v33, v65
	v_fma_f32 v40, -v40, v66, v43
	s_nop 1
	v_mov_b32_dpp v43, v33 quad_perm:[2,3,0,1] row_mask:0xf bank_mask:0xf
	v_div_fmas_f32 v40, v40, v42, v66
	v_mul_f32_e32 v38, v4, v38
	v_div_fixup_f32 v39, v40, v39, v69
	v_mul_f32_e32 v38, v39, v38
	s_waitcnt lgkmcnt(0)
	v_add_f32_e32 v33, v33, v43
	s_nop 1
	v_mov_b32_dpp v43, v33 row_half_mirror row_mask:0xf bank_mask:0xf
	v_mul_f32_e32 v39, v41, v45
	v_mul_f32_e32 v42, 0xbfb8aa3b, v37
	v_exp_f32_e32 v42, v42
	v_mul_f32_e32 v39, v5, v39
	s_waitcnt lgkmcnt(0)
	v_add_f32_e32 v33, v33, v43
	s_nop 1
	v_mov_b32_dpp v41, v33 row_mirror row_mask:0xf bank_mask:0xf
	v_add_f32_e32 v40, 1.0, v42
	v_div_scale_f32 v42, s[0:1], v40, v40, v37
	v_rcp_f32_e32 v43, v42
	s_waitcnt lgkmcnt(0)
	v_add_f32_e32 v33, v33, v41
	v_mov_b32_e32 v41, v33
	v_mov_b32_e32 v61, v33
	s_nop 1
	v_permlane16_swap_b32_e32 v41, v61
	s_nop 1
	v_mov_b32_dpp v41, v61 quad_perm:[0,1,2,3] row_mask:0x5 bank_mask:0xf
	v_fma_f32 v45, -v42, v43, 1.0
	v_fmac_f32_e32 v43, v45, v43
	v_div_scale_f32 v45, vcc, v37, v40, v37
	s_waitcnt lgkmcnt(0)
	v_add_f32_e32 v33, v33, v41
	v_mov_b32_e32 v41, v33
	v_mov_b32_e32 v62, v33
	s_nop 1
	v_permlane32_swap_b32_e32 v41, v62
	s_nop 1
	v_mov_b32_dpp v41, v62 quad_perm:[0,1,2,3] row_mask:0x3 bank_mask:0xf
	v_mul_f32_e32 v65, v45, v43
	v_fma_f32 v66, -v42, v65, v45
	v_fmac_f32_e32 v65, v66, v43
	v_fma_f32 v42, -v42, v65, v45
	s_waitcnt lgkmcnt(0)
	v_add_f32_e32 v33, v33, v41
	v_fmamk_f32 v33, v33, 0x3b000000, v57
	v_mul_f32_e32 v41, 0x4f800000, v33
	v_cmp_gt_f32_e64 s[0:1], s2, v33
	v_div_fmas_f32 v42, v42, v43, v65
	v_div_fixup_f32 v37, v42, v40, v37
	v_cndmask_b32_e64 v33, v33, v41, s[0:1]
	v_sqrt_f32_e32 v41, v33
	v_mul_f32_e32 v37, v37, v39
	v_cvt_pk_bf16_f32 v37, v38, v37
	global_store_dwordx4 v[46:47], v[34:37], off offset:1024
	v_add_u32_e32 v40, -1, v41
	v_fma_f32 v42, -v40, v41, v33
	v_cmp_ge_f32_e32 vcc, 0, v42
	v_add_u32_e32 v42, 1, v41
	v_lshlrev_b32_e32 v37, 16, v24
	v_cndmask_b32_e32 v40, v41, v40, vcc
	v_fma_f32 v41, -v42, v41, v33
	v_cmp_lt_f32_e32 vcc, 0, v41
	v_and_b32_e32 v24, 0xffff0000, v24
	v_lshlrev_b32_e32 v38, 16, v25
	v_cndmask_b32_e32 v40, v40, v42, vcc
	v_mul_f32_e32 v41, 0x37800000, v40
	v_cndmask_b32_e64 v40, v40, v41, s[0:1]
	v_cmp_class_f32_e32 vcc, v33, v58
	v_and_b32_e32 v25, 0xffff0000, v25
	s_nop 0
	v_cndmask_b32_e32 v33, v40, v33, vcc
	v_div_scale_f32 v40, s[0:1], v33, v33, 1.0
	v_rcp_f32_e32 v41, v40
	s_nop 0
	v_fma_f32 v34, -v40, v41, 1.0
	v_fmac_f32_e32 v41, v34, v41
	v_div_scale_f32 v34, vcc, 1.0, v33, 1.0
	v_mul_f32_e32 v35, v34, v41
	v_fma_f32 v36, -v40, v35, v34
	v_fmac_f32_e32 v35, v36, v41
	v_fma_f32 v34, -v40, v35, v34
	v_div_fmas_f32 v34, v34, v41, v35
	v_div_fixup_f32 v33, v34, v33, 1.0
	v_lshlrev_b32_e32 v34, 16, v22
	v_mul_f32_e32 v36, 0xbfb8aa3b, v34
	v_exp_f32_e32 v36, v36
	v_mul_f32_e32 v41, v44, v33
	v_and_b32_e32 v22, 0xffff0000, v22
	v_mul_f32_e32 v41, v6, v41
	v_add_f32_e32 v36, 1.0, v36
	v_div_scale_f32 v39, s[0:1], v36, v36, v34
	v_rcp_f32_e32 v40, v39
	v_lshlrev_b32_e32 v35, 16, v23
	v_mul_f32_e32 v26, v26, v33
	v_mul_f32_e32 v26, v7, v26
	v_fma_f32 v42, -v39, v40, 1.0
	v_fmac_f32_e32 v40, v42, v40
	v_div_scale_f32 v42, vcc, v34, v36, v34
	v_mul_f32_e32 v43, v42, v40
	v_fma_f32 v44, -v39, v43, v42
	v_fmac_f32_e32 v43, v44, v40
	v_fma_f32 v39, -v39, v43, v42
	v_mul_f32_e32 v42, 0xbfb8aa3b, v22
	v_exp_f32_e32 v42, v42
	v_div_fmas_f32 v39, v39, v40, v43
	v_div_fixup_f32 v34, v39, v36, v34
	v_mul_f32_e32 v34, v34, v41
	v_add_f32_e32 v36, 1.0, v42
	v_div_scale_f32 v39, s[0:1], v36, v36, v22
	v_rcp_f32_e32 v40, v39
	v_and_b32_e32 v23, 0xffff0000, v23
	v_mul_f32_e32 v30, v30, v33
	v_mul_f32_e32 v30, v8, v30
	v_fma_f32 v41, -v39, v40, 1.0
	v_fmac_f32_e32 v40, v41, v40
	v_div_scale_f32 v41, vcc, v22, v36, v22
	v_mul_f32_e32 v42, v41, v40
	v_fma_f32 v43, -v39, v42, v41
	v_fmac_f32_e32 v42, v43, v40
	v_fma_f32 v39, -v39, v42, v41
	v_mul_f32_e32 v41, 0xbfb8aa3b, v35
	v_exp_f32_e32 v41, v41
	v_div_fmas_f32 v39, v39, v40, v42
	v_div_fixup_f32 v22, v39, v36, v22
	v_mul_f32_e32 v22, v22, v26
	v_add_f32_e32 v26, 1.0, v41
	v_div_scale_f32 v36, s[0:1], v26, v26, v35
	v_rcp_f32_e32 v39, v36
	v_cvt_pk_bf16_f32 v22, v34, v22
	v_mul_f32_e32 v27, v27, v33
	v_mul_f32_e32 v27, v9, v27
	v_fma_f32 v34, -v36, v39, 1.0
	v_fmac_f32_e32 v39, v34, v39
	v_div_scale_f32 v34, vcc, v35, v26, v35
	v_mul_f32_e32 v40, v34, v39
	v_fma_f32 v41, -v36, v40, v34
	v_fmac_f32_e32 v40, v41, v39
	v_fma_f32 v34, -v36, v40, v34
	v_mul_f32_e32 v36, 0xbfb8aa3b, v23
	v_exp_f32_e32 v36, v36
	v_div_fmas_f32 v34, v34, v39, v40
	v_div_fixup_f32 v26, v34, v26, v35
	v_mul_f32_e32 v26, v26, v30
	v_add_f32_e32 v34, 1.0, v36
	v_div_scale_f32 v35, s[0:1], v34, v34, v23
	v_rcp_f32_e32 v36, v35
	s_nop 0
	v_fma_f32 v30, -v35, v36, 1.0
	v_fmac_f32_e32 v36, v30, v36
	v_div_scale_f32 v30, vcc, v23, v34, v23
	v_mul_f32_e32 v39, v30, v36
	v_fma_f32 v40, -v35, v39, v30
	v_fmac_f32_e32 v39, v40, v36
	v_fma_f32 v30, -v35, v39, v30
	v_mul_f32_e32 v35, 0xbfb8aa3b, v37
	v_exp_f32_e32 v35, v35
	v_div_fmas_f32 v30, v30, v36, v39
	v_div_fixup_f32 v23, v30, v34, v23
	v_mul_f32_e32 v23, v23, v27
	v_add_f32_e32 v27, 1.0, v35
	v_div_scale_f32 v30, s[0:1], v27, v27, v37
	v_rcp_f32_e32 v34, v30
	v_cvt_pk_bf16_f32 v23, v26, v23
	v_mul_f32_e32 v26, v31, v33
	v_mul_f32_e32 v26, v2, v26
	v_fma_f32 v31, -v30, v34, 1.0
	v_fmac_f32_e32 v34, v31, v34
	v_div_scale_f32 v31, vcc, v37, v27, v37
	v_mul_f32_e32 v35, v31, v34
	v_fma_f32 v36, -v30, v35, v31
	v_fmac_f32_e32 v35, v36, v34
	v_fma_f32 v30, -v30, v35, v31
	v_mul_f32_e32 v31, 0xbfb8aa3b, v24
	v_exp_f32_e32 v31, v31
	v_div_fmas_f32 v30, v30, v34, v35
	v_div_fixup_f32 v27, v30, v27, v37
	v_mul_f32_e32 v26, v27, v26
	v_add_f32_e32 v30, 1.0, v31
	v_div_scale_f32 v31, s[0:1], v30, v30, v24
	v_rcp_f32_e32 v34, v31
	v_mul_f32_e32 v27, v28, v33
	v_mul_f32_e32 v27, v3, v27
	v_fma_f32 v28, -v31, v34, 1.0
	v_fmac_f32_e32 v34, v28, v34
	v_div_scale_f32 v28, vcc, v24, v30, v24
	v_mul_f32_e32 v35, v28, v34
	v_fma_f32 v36, -v31, v35, v28
	v_fmac_f32_e32 v35, v36, v34
	v_fma_f32 v28, -v31, v35, v28
	v_div_fmas_f32 v28, v28, v34, v35
	v_div_fixup_f32 v24, v28, v30, v24
	v_mul_f32_e32 v24, v24, v27
	v_cvt_pk_bf16_f32 v24, v26, v24
	v_mul_f32_e32 v26, v32, v33
	v_lshlrev_b32_e32 v32, 16, v14
	v_lshlrev_b32_e32 v34, 16, v18
	v_and_b32_e32 v18, 0xffff0000, v18
	v_and_b32_e32 v14, 0xffff0000, v14
	v_add_f32_e32 v32, v34, v32
	v_add_f32_e32 v14, v18, v14
	v_lshlrev_b32_e32 v18, 16, v15
	v_lshlrev_b32_e32 v34, 16, v19
	v_and_b32_e32 v19, 0xffff0000, v19
	v_and_b32_e32 v15, 0xffff0000, v15
	v_mul_f32_e32 v31, 0xbfb8aa3b, v38
	v_add_f32_e32 v18, v34, v18
	v_add_f32_e32 v15, v19, v15
	v_lshlrev_b32_e32 v19, 16, v16
	v_lshlrev_b32_e32 v34, 16, v20
	v_and_b32_e32 v20, 0xffff0000, v20
	v_and_b32_e32 v16, 0xffff0000, v16
	v_exp_f32_e32 v31, v31
	v_add_f32_e32 v19, v34, v19
	v_add_f32_e32 v16, v20, v16
	v_lshlrev_b32_e32 v20, 16, v17
	v_lshlrev_b32_e32 v34, 16, v21
	v_and_b32_e32 v21, 0xffff0000, v21
	v_and_b32_e32 v17, 0xffff0000, v17
	v_add_f32_e32 v17, v21, v17
	v_mul_f32_e32 v21, v32, v32
	v_fmac_f32_e32 v21, v14, v14
	v_fmac_f32_e32 v21, v18, v18
	v_add_f32_e32 v27, 1.0, v31
	v_fmac_f32_e32 v21, v15, v15
	v_div_scale_f32 v28, s[0:1], v27, v27, v38
	v_fmac_f32_e32 v21, v19, v19
	v_rcp_f32_e32 v30, v28
	v_add_f32_e32 v20, v34, v20
	v_fmac_f32_e32 v21, v16, v16
	v_fmac_f32_e32 v21, v20, v20
	v_fmac_f32_e32 v21, v17, v17
	s_nop 1
	v_mov_b32_dpp v34, v21 quad_perm:[1,0,3,2] row_mask:0xf bank_mask:0xf
	v_fma_f32 v31, -v28, v30, 1.0
	v_fmac_f32_e32 v30, v31, v30
	v_div_scale_f32 v31, vcc, v38, v27, v38
	v_mul_f32_e32 v35, v31, v30
	v_fma_f32 v36, -v28, v35, v31
	v_fmac_f32_e32 v35, v36, v30
	s_waitcnt lgkmcnt(0)
	v_add_f32_e32 v21, v21, v34
	v_fma_f32 v28, -v28, v35, v31
	s_nop 1
	v_mov_b32_dpp v31, v21 quad_perm:[2,3,0,1] row_mask:0xf bank_mask:0xf
	v_div_fmas_f32 v28, v28, v30, v35
	v_mul_f32_e32 v26, v4, v26
	v_div_fixup_f32 v27, v28, v27, v38
	v_mul_f32_e32 v26, v27, v26
	s_waitcnt lgkmcnt(0)
	v_add_f32_e32 v21, v21, v31
	s_nop 1
	v_mov_b32_dpp v31, v21 row_half_mirror row_mask:0xf bank_mask:0xf
	v_mul_f32_e32 v27, v29, v33
	v_mul_f32_e32 v30, 0xbfb8aa3b, v25
	v_exp_f32_e32 v30, v30
	v_mul_f32_e32 v27, v5, v27
	s_waitcnt lgkmcnt(0)
	v_add_f32_e32 v21, v21, v31
	s_nop 1
	v_mov_b32_dpp v29, v21 row_mirror row_mask:0xf bank_mask:0xf
	v_add_f32_e32 v28, 1.0, v30
	v_div_scale_f32 v30, s[0:1], v28, v28, v25
	v_rcp_f32_e32 v31, v30
	s_waitcnt lgkmcnt(0)
	v_add_f32_e32 v21, v21, v29
	v_mov_b32_e32 v29, v21
	v_mov_b32_e32 v61, v21
	s_nop 1
	v_permlane16_swap_b32_e32 v29, v61
	s_nop 1
	v_mov_b32_dpp v29, v61 quad_perm:[0,1,2,3] row_mask:0x5 bank_mask:0xf
	v_fma_f32 v33, -v30, v31, 1.0
	v_fmac_f32_e32 v31, v33, v31
	v_div_scale_f32 v33, vcc, v25, v28, v25
	s_waitcnt lgkmcnt(0)
	v_add_f32_e32 v21, v21, v29
	v_mov_b32_e32 v29, v21
	v_mov_b32_e32 v62, v21
	s_nop 1
	v_permlane32_swap_b32_e32 v29, v62
	s_nop 1
	v_mov_b32_dpp v29, v62 quad_perm:[0,1,2,3] row_mask:0x3 bank_mask:0xf
	v_mul_f32_e32 v34, v33, v31
	v_fma_f32 v35, -v30, v34, v33
	v_fmac_f32_e32 v34, v35, v31
	v_fma_f32 v30, -v30, v34, v33
	s_waitcnt lgkmcnt(0)
	v_add_f32_e32 v21, v21, v29
	v_fmamk_f32 v21, v21, 0x3b000000, v57
	v_mul_f32_e32 v29, 0x4f800000, v21
	v_cmp_gt_f32_e64 s[0:1], s2, v21
	v_div_fmas_f32 v30, v30, v31, v34
	v_div_fixup_f32 v25, v30, v28, v25
	v_cndmask_b32_e64 v21, v21, v29, s[0:1]
	v_sqrt_f32_e32 v29, v21
	v_mul_f32_e32 v25, v25, v27
	v_cvt_pk_bf16_f32 v25, v26, v25
	global_store_dwordx4 v[46:47], v[22:25], off offset:2048
	v_add_u32_e32 v28, -1, v29
	v_fma_f32 v30, -v28, v29, v21
	v_cmp_ge_f32_e32 vcc, 0, v30
	v_add_u32_e32 v30, 1, v29
	v_lshlrev_b32_e32 v25, 16, v12
	v_cndmask_b32_e32 v28, v29, v28, vcc
	v_fma_f32 v29, -v30, v29, v21
	v_cmp_lt_f32_e32 vcc, 0, v29
	v_and_b32_e32 v12, 0xffff0000, v12
	v_lshlrev_b32_e32 v26, 16, v13
	v_cndmask_b32_e32 v28, v28, v30, vcc
	v_mul_f32_e32 v29, 0x37800000, v28
	v_cndmask_b32_e64 v28, v28, v29, s[0:1]
	v_cmp_class_f32_e32 vcc, v21, v58
	v_and_b32_e32 v13, 0xffff0000, v13
	s_nop 0
	v_cndmask_b32_e32 v21, v28, v21, vcc
	v_div_scale_f32 v28, s[0:1], v21, v21, 1.0
	v_rcp_f32_e32 v29, v28
	s_nop 0
	v_fma_f32 v22, -v28, v29, 1.0
	v_fmac_f32_e32 v29, v22, v29
	v_div_scale_f32 v22, vcc, 1.0, v21, 1.0
	v_mul_f32_e32 v23, v22, v29
	v_fma_f32 v24, -v28, v23, v22
	v_fmac_f32_e32 v23, v24, v29
	v_fma_f32 v22, -v28, v23, v22
	v_div_fmas_f32 v22, v22, v29, v23
	v_div_fixup_f32 v21, v22, v21, 1.0
	v_lshlrev_b32_e32 v22, 16, v10
	v_mul_f32_e32 v24, 0xbfb8aa3b, v22
	v_exp_f32_e32 v24, v24
	v_mul_f32_e32 v29, v32, v21
	v_mul_f32_e32 v6, v6, v29
	v_and_b32_e32 v10, 0xffff0000, v10
	v_add_f32_e32 v24, 1.0, v24
	v_div_scale_f32 v27, s[0:1], v24, v24, v22
	v_rcp_f32_e32 v28, v27
	v_mul_f32_e32 v14, v14, v21
	v_mul_f32_e32 v7, v7, v14
	v_lshlrev_b32_e32 v23, 16, v11
	v_fma_f32 v29, -v27, v28, 1.0
	v_fmac_f32_e32 v28, v29, v28
	v_div_scale_f32 v29, vcc, v22, v24, v22
	v_mul_f32_e32 v30, v29, v28
	v_fma_f32 v31, -v27, v30, v29
	v_fmac_f32_e32 v30, v31, v28
	v_fma_f32 v27, -v27, v30, v29
	v_mul_f32_e32 v29, 0xbfb8aa3b, v10
	v_exp_f32_e32 v29, v29
	v_div_fmas_f32 v27, v27, v28, v30
	v_div_fixup_f32 v22, v27, v24, v22
	v_mul_f32_e32 v6, v22, v6
	v_add_f32_e32 v24, 1.0, v29
	v_div_scale_f32 v27, s[0:1], v24, v24, v10
	v_rcp_f32_e32 v28, v27
	v_and_b32_e32 v11, 0xffff0000, v11
	v_fma_f32 v14, -v27, v28, 1.0
	v_fmac_f32_e32 v28, v14, v28
	v_div_scale_f32 v14, vcc, v10, v24, v10
	v_mul_f32_e32 v22, v14, v28
	v_fma_f32 v29, -v27, v22, v14
	v_fmac_f32_e32 v22, v29, v28
	v_fma_f32 v14, -v27, v22, v14
	v_mul_f32_e32 v27, 0xbfb8aa3b, v23
	v_exp_f32_e32 v27, v27
	v_div_fmas_f32 v14, v14, v28, v22
	v_div_fixup_f32 v10, v14, v24, v10
	v_mul_f32_e32 v7, v10, v7
	v_add_f32_e32 v10, 1.0, v27
	v_div_scale_f32 v14, s[0:1], v10, v10, v23
	v_rcp_f32_e32 v22, v14
	v_cvt_pk_bf16_f32 v6, v6, v7
	v_mul_f32_e32 v7, v18, v21
	v_mul_f32_e32 v7, v8, v7
	v_fma_f32 v8, -v14, v22, 1.0
	v_fmac_f32_e32 v22, v8, v22
	v_div_scale_f32 v8, vcc, v23, v10, v23
	v_mul_f32_e32 v18, v8, v22
	v_fma_f32 v24, -v14, v18, v8
	v_fmac_f32_e32 v18, v24, v22
	v_fma_f32 v8, -v14, v18, v8
	v_mul_f32_e32 v14, 0xbfb8aa3b, v11
	v_exp_f32_e32 v14, v14
	v_div_fmas_f32 v8, v8, v22, v18
	v_div_fixup_f32 v8, v8, v10, v23
	v_mul_f32_e32 v7, v8, v7
	v_add_f32_e32 v10, 1.0, v14
	v_div_scale_f32 v14, s[0:1], v10, v10, v11
	v_rcp_f32_e32 v18, v14
	v_mul_f32_e32 v8, v15, v21
	v_mul_f32_e32 v8, v9, v8
	v_fma_f32 v9, -v14, v18, 1.0
	v_fmac_f32_e32 v18, v9, v18
	v_div_scale_f32 v9, vcc, v11, v10, v11
	v_mul_f32_e32 v15, v9, v18
	v_fma_f32 v22, -v14, v15, v9
	v_fmac_f32_e32 v15, v22, v18
	v_fma_f32 v9, -v14, v15, v9
	v_mul_f32_e32 v14, 0xbfb8aa3b, v25
	v_exp_f32_e32 v14, v14
	v_div_fmas_f32 v9, v9, v18, v15
	v_div_fixup_f32 v9, v9, v10, v11
	v_mul_f32_e32 v8, v9, v8
	v_add_f32_e32 v9, 1.0, v14
	v_div_scale_f32 v10, s[0:1], v9, v9, v25
	v_rcp_f32_e32 v11, v10
	v_cvt_pk_bf16_f32 v7, v7, v8
	v_mul_f32_e32 v8, v19, v21
	v_mul_f32_e32 v2, v2, v8
	v_fma_f32 v8, -v10, v11, 1.0
	v_fmac_f32_e32 v11, v8, v11
	v_div_scale_f32 v8, vcc, v25, v9, v25
	v_mul_f32_e32 v14, v8, v11
	v_fma_f32 v15, -v10, v14, v8
	v_fmac_f32_e32 v14, v15, v11
	v_fma_f32 v8, -v10, v14, v8
	v_mul_f32_e32 v10, 0xbfb8aa3b, v12
	v_exp_f32_e32 v10, v10
	v_div_fmas_f32 v8, v8, v11, v14
	v_div_fixup_f32 v8, v8, v9, v25
	v_mul_f32_e32 v2, v8, v2
	v_add_f32_e32 v9, 1.0, v10
	v_div_scale_f32 v10, s[0:1], v9, v9, v12
	v_rcp_f32_e32 v11, v10
	v_mul_f32_e32 v8, v16, v21
	v_mul_f32_e32 v3, v3, v8
	v_fma_f32 v8, -v10, v11, 1.0
	v_fmac_f32_e32 v11, v8, v11
	v_div_scale_f32 v8, vcc, v12, v9, v12
	v_mul_f32_e32 v14, v8, v11
	v_fma_f32 v15, -v10, v14, v8
	v_fmac_f32_e32 v14, v15, v11
	v_fma_f32 v8, -v10, v14, v8
	v_mul_f32_e32 v10, 0xbfb8aa3b, v26
	v_exp_f32_e32 v10, v10
	v_div_fmas_f32 v8, v8, v11, v14
	v_div_fixup_f32 v8, v8, v9, v12
	v_mul_f32_e32 v3, v8, v3
	v_add_f32_e32 v9, 1.0, v10
	v_div_scale_f32 v10, s[0:1], v9, v9, v26
	v_rcp_f32_e32 v11, v10
	v_cvt_pk_bf16_f32 v8, v2, v3
	v_mul_f32_e32 v2, v20, v21
	v_mul_f32_e32 v2, v4, v2
	v_fma_f32 v3, -v10, v11, 1.0
	v_fmac_f32_e32 v11, v3, v11
	v_div_scale_f32 v3, vcc, v26, v9, v26
	v_mul_f32_e32 v4, v3, v11
	v_fma_f32 v12, -v10, v4, v3
	v_fmac_f32_e32 v4, v12, v11
	v_fma_f32 v3, -v10, v4, v3
	v_mul_f32_e32 v10, 0xbfb8aa3b, v13
	v_exp_f32_e32 v10, v10
	v_div_fmas_f32 v3, v3, v11, v4
	v_div_fixup_f32 v3, v3, v9, v26
	v_mul_f32_e32 v2, v3, v2
	v_add_f32_e32 v4, 1.0, v10
	v_div_scale_f32 v9, s[0:1], v4, v4, v13
	v_rcp_f32_e32 v10, v9
	v_mul_f32_e32 v3, v17, v21
	v_mul_f32_e32 v3, v5, v3
	v_fma_f32 v5, -v9, v10, 1.0
	v_fmac_f32_e32 v10, v5, v10
	v_div_scale_f32 v5, vcc, v13, v4, v13
	v_mul_f32_e32 v11, v5, v10
	v_fma_f32 v12, -v9, v11, v5
	v_fmac_f32_e32 v11, v12, v10
	v_fma_f32 v5, -v9, v11, v5
	v_div_fmas_f32 v5, v5, v10, v11
	v_div_fixup_f32 v4, v5, v4, v13
	v_mul_f32_e32 v3, v4, v3
	v_cvt_pk_bf16_f32 v9, v2, v3
	global_store_dwordx4 v[46:47], v[6:9], off offset:3072
	s_cbranch_scc1 .LBB0_817
